# gemm prologues issue tile-1 staging loads before first wait (one exposed latency instead of two); grid-barrier XCD leader releases local generation before its own L1 invalidate
# speedup vs baseline: 1.0022x; 1.0022x over previous
.LBB0_128:
	s_or_b64 exec, exec, s[8:9]
	s_mov_b64 s[2:3], exec
	v_mbcnt_lo_u32_b32 v1, s2, 0
	v_mbcnt_hi_u32_b32 v1, s3, v1
	v_cmp_eq_u32_e32 vcc, 0, v1
	s_waitcnt vmcnt(0)
	s_and_saveexec_b64 s[8:9], vcc
	s_cbranch_execz .LBB0_130
	s_bcnt1_i32_b64 s2, s[2:3]
	v_mov_b32_e32 v1, 0x2000
	v_mov_b32_e32 v2, s2
	global_atomic_add v1, v2, s[6:7] offset:1024
	buffer_inv sc1

.LBB0_168:
	v_bfe_u32 v17, v10, 4, 2
	v_and_b32_e32 v205, 15, v10
	v_lshlrev_b32_e32 v19, 4, v17
	v_lshlrev_b32_e32 v10, 2, v10
	s_lshl_b32 s7, s5, 8
	s_and_b32 s5, s8, 3
	s_lshl_b32 s93, s6, 6
	v_lshl_or_b32 v19, v205, 6, v19
	s_lshl_b32 s6, s6, 13
	v_and_b32_e32 v10, 32, v10
	s_lshl_b32 s72, s33, 3
	v_bitop3_b32 v20, v19, s6, v10 bitop3:0xde
	s_lshl_b32 s6, s5, 12
	s_lshl_b64 s[8:9], s[72:73], 2
	s_waitcnt lgkmcnt(0)
	s_add_u32 s94, s36, s8
	s_addc_u32 s95, s37, s9
	s_add_i32 m0, s85, 0x18000
	v_lshl_add_u64 v[8:9], v[8:9], 0, s[60:61]
	global_load_lds_dwordx4 v[8:9], off
	v_lshl_add_u64 v[6:7], v[6:7], 0, s[60:61]
	s_add_i32 m0, s85, 0x1a000
	s_add_i32 s96, s85, 0x8000
	s_add_i32 s97, s85, 0xa000
	global_load_lds_dwordx4 v[6:7], off
	v_lshl_add_u64 v[2:3], v[2:3], 0, s[60:61]
	s_mov_b32 m0, s96
	s_add_u32 s8, s38, 0x40080
	global_load_lds_dwordx4 v[2:3], off
	v_lshl_add_u64 v[2:3], v[4:5], 0, s[60:61]
	s_mov_b32 m0, s97
	s_addc_u32 s9, s39, 0
	global_load_lds_dwordx4 v[2:3], off
	s_add_i32 m0, s85, 0x1c000
	v_lshl_add_u64 v[2:3], s[8:9], 0, v[210:211]
	global_load_lds_dwordx4 v[2:3], off
	v_lshl_add_u64 v[2:3], s[8:9], 0, v[214:215]
	s_add_i32 m0, s85, 0x1e000
	v_lshlrev_b32_e32 v18, 3, v17
	global_load_lds_dwordx4 v[2:3], off
	s_mov_b64 vcc, s[46:47]
	s_cbranch_vccz .Lpro_skip_0
	s_barrier
.Lpro_skip_0:
	s_waitcnt vmcnt(8)
	s_barrier
	v_or_b32_e32 v2, 16, v205
	v_cmp_eq_u32_e32 vcc, v18, v205
	v_mov_b32_e32 v28, 0x3f80
	v_or_b32_e32 v4, 1, v18
	v_cndmask_b32_e32 v6, 0, v28, vcc
	v_cmp_eq_u32_e32 vcc, v18, v2
	v_bitop3_b32 v219, v19, s6, v10 bitop3:0xde
	v_or_b32_e32 v3, 2, v18
	v_cndmask_b32_e32 v10, 0, v28, vcc
	v_cmp_eq_u32_e32 vcc, v4, v205
	s_cmpk_lt_u32 s4, 0x100
	s_cselect_b64 s[48:49], -1, 0
	v_cndmask_b32_e32 v7, 0, v28, vcc
	v_cmp_eq_u32_e32 vcc, v3, v205
	v_lshl_or_b32 v216, s5, 5, v18
	s_lshl_b32 s4, s5, 14
	v_cndmask_b32_e32 v5, 0, v28, vcc
	v_cmp_eq_u32_e32 vcc, v4, v2
	v_or_b32_e32 v4, 3, v18
	s_mov_b32 s5, 0x5040100
	v_cndmask_b32_e32 v19, 0, v28, vcc
	v_cmp_eq_u32_e32 vcc, v3, v2
	v_or_b32_e32 v3, 4, v18
	s_waitcnt vmcnt(6)
	v_or_b32_e32 v217, s93, v205
	v_cndmask_b32_e32 v9, 0, v28, vcc
	v_cmp_eq_u32_e32 vcc, v4, v205
	v_or_b32_e32 v236, 16, v217
	v_or_b32_e32 v237, 32, v217
	v_cndmask_b32_e32 v8, 0, v28, vcc
	v_cmp_eq_u32_e32 vcc, v3, v205
	v_or_b32_e32 v238, 48, v217
	v_add_u32_e32 v239, 0x80, v217
	v_cndmask_b32_e32 v21, 0, v28, vcc
	v_cmp_eq_u32_e32 vcc, v4, v2
	v_or_b32_e32 v4, 5, v18
	v_add_u32_e32 v240, 0x90, v217
	v_cndmask_b32_e32 v22, 0, v28, vcc
	v_cmp_eq_u32_e32 vcc, v3, v2
	v_or_b32_e32 v3, 6, v18
	v_add_u32_e32 v241, 0xa0, v217
	v_cndmask_b32_e32 v23, 0, v28, vcc
	v_cmp_eq_u32_e32 vcc, v3, v205
	v_add_u32_e32 v242, 0xb0, v217
	v_lshlrev_b32_e32 v243, 2, v17
	v_cndmask_b32_e32 v24, 0, v28, vcc
	v_cmp_eq_u32_e32 vcc, v4, v205
	v_lshlrev_b32_e32 v218, 3, v205
	v_mov_b32_e32 v221, v67
	v_cndmask_b32_e32 v25, 0, v28, vcc
	v_cmp_eq_u32_e32 vcc, v3, v2
	v_or_b32_e32 v3, 7, v18
	v_mov_b32_e32 v223, v67
	v_cndmask_b32_e32 v26, 0, v28, vcc
	v_cmp_eq_u32_e32 vcc, v4, v2
	v_perm_b32 v4, v25, v21, s5
	s_mov_b64 s[36:37], 0
	v_cndmask_b32_e32 v27, 0, v28, vcc
	v_cmp_eq_u32_e32 vcc, v3, v205
	v_add_u32_e32 v244, 0, v20
	s_mov_b64 s[56:57], s[38:39]
	v_cndmask_b32_e32 v18, 0, v28, vcc
	v_cmp_eq_u32_e32 vcc, v3, v2
	v_perm_b32 v2, v7, v6, s5
	v_perm_b32 v6, v19, v10, s5
	v_lshlrev_b32_e32 v10, 14, v11
	v_and_b32_e32 v10, 0xffff8000, v10
	v_lshl_add_u32 v10, v12, 11, v10
	v_and_b32_e32 v11, 1, v11
	v_lshl_or_b32 v10, v11, 6, v10
	v_lshl_add_u32 v220, v13, 1, v10
	v_lshlrev_b32_e32 v10, 14, v14
	v_and_b32_e32 v10, 0xffff8000, v10
	v_lshl_add_u32 v10, v15, 11, v10
	v_and_b32_e32 v11, 1, v14
	v_cndmask_b32_e32 v28, 0, v28, vcc
	v_lshl_or_b32 v10, v11, 6, v10
	v_perm_b32 v3, v8, v5, s5
	v_perm_b32 v5, v18, v24, s5
	v_perm_b32 v8, v27, v23, s5
	v_perm_b32 v7, v22, v9, s5
	v_perm_b32 v9, v28, v26, s5
	v_lshl_add_u32 v222, v16, 1, v10
	s_mov_b64 s[54:55], s[34:35]
	s_barrier
	s_branch .LBB0_171

.LBB0_406:
	s_or_b64 exec, exec, s[36:37]
	s_mov_b64 s[26:27], exec
	v_mbcnt_lo_u32_b32 v2, s26, 0
	v_mbcnt_hi_u32_b32 v2, s27, v2
	v_cmp_eq_u32_e32 vcc, 0, v2
	s_waitcnt vmcnt(0)
	s_and_saveexec_b64 s[36:37], vcc
	s_cbranch_execz .LBB0_408
	s_bcnt1_i32_b64 s3, s[26:27]
	v_readlane_b32 s4, v254, 7
	v_mov_b32_e32 v2, s3
	v_readlane_b32 s5, v254, 8
	s_nop 4
	global_atomic_add v67, v2, s[4:5]
	buffer_inv sc1

.LBB0_477:
	v_lshrrev_b32_e32 v12, 1, v10
	v_and_b32_e32 v12, 24, v12
	v_and_b32_e32 v11, 15, v10
	v_lshlrev_b32_e32 v13, 1, v12
	v_lshlrev_b32_e32 v10, 2, v10
	s_lshl_b32 s9, s9, 5
	v_lshl_or_b32 v197, s10, 6, v11
	v_lshl_or_b32 v11, v11, 6, v13
	s_lshl_b32 s10, s10, 13
	v_and_b32_e32 v10, 32, v10
	s_and_b32 s9, s9, 0x60
	v_bitop3_b32 v13, v11, s10, v10 bitop3:0xde
	s_lshl_b32 s10, s9, 7
	s_and_b32 s35, s11, 3
	s_add_u32 s40, s74, 0xea00000
	s_addc_u32 s41, s75, 0
	s_add_i32 m0, s91, 0x18000
	v_lshl_add_u64 v[8:9], v[8:9], 0, s[60:61]
	global_load_lds_dwordx4 v[8:9], off
	v_lshl_add_u64 v[6:7], v[6:7], 0, s[60:61]
	s_add_i32 m0, s91, 0x1a000
	s_add_i32 s65, s91, 0x8000
	s_add_i32 s68, s91, 0xa000
	v_bitop3_b32 v211, v11, s10, v10 bitop3:0xde
	global_load_lds_dwordx4 v[6:7], off
	v_lshl_add_u64 v[2:3], v[2:3], 0, s[60:61]
	s_mov_b32 m0, s65
	s_add_u32 s10, s52, 0x40080
	global_load_lds_dwordx4 v[2:3], off
	v_lshl_add_u64 v[2:3], v[4:5], 0, s[60:61]
	s_mov_b32 m0, s68
	s_addc_u32 s11, s53, 0
	global_load_lds_dwordx4 v[2:3], off
	s_add_i32 m0, s91, 0x1c000
	v_lshl_add_u64 v[2:3], s[10:11], 0, v[200:201]
	global_load_lds_dwordx4 v[2:3], off
	v_lshl_add_u64 v[2:3], s[10:11], 0, v[208:209]
	s_add_i32 m0, s91, 0x1e000
	s_cmpk_lt_u32 s8, 0x100
	global_load_lds_dwordx4 v[2:3], off
	s_mov_b64 vcc, s[38:39]
	s_cbranch_vccz .Lpro_skip_1
	s_barrier
.Lpro_skip_1:
	s_waitcnt vmcnt(8)
	s_barrier
	s_waitcnt vmcnt(6)
	s_cselect_b64 s[42:43], -1, 0
	v_or_b32_e32 v210, s9, v12
	v_or_b32_e32 v220, 16, v197
	v_or_b32_e32 v221, 32, v197
	v_or_b32_e32 v222, 48, v197
	v_add_u32_e32 v223, 0x80, v197
	v_add_u32_e32 v225, 0x90, v197
	v_add_u32_e32 v226, 0xa0, v197
	v_add_u32_e32 v227, 0xb0, v197
	s_mov_b64 s[56:57], 0
	v_add_u32_e32 v228, 0, v13
	s_mov_b64 s[48:49], s[52:53]
	s_mov_b64 s[46:47], s[54:55]
	s_barrier
	s_branch .LBB0_480

.LBB0_501:
	v_bfe_u32 v13, v12, 4, 2
	v_and_b32_e32 v14, 15, v12
	v_lshlrev_b32_e32 v15, 3, v13
	v_lshlrev_b32_e32 v13, 4, v13
	v_lshlrev_b32_e32 v12, 2, v12
	s_and_b32 s26, s10, 3
	v_lshl_or_b32 v197, s9, 6, v14
	v_lshl_or_b32 v13, v14, 6, v13
	s_lshl_b32 s9, s9, 13
	v_and_b32_e32 v12, 32, v12
	v_bitop3_b32 v14, v13, s9, v12 bitop3:0xde
	s_lshl_b32 s9, s26, 12
	s_lshl_b32 s87, s13, 8
	s_lshl_b32 s88, s14, 8
	s_add_u32 s14, s11, 0x800080
	v_mov_b32_e32 v199, v67
	s_addc_u32 s15, s12, 0
	v_mov_b32_e32 v203, v67
	v_bitop3_b32 v205, v13, s9, v12 bitop3:0xde
	s_add_i32 m0, s58, 0x18000
	v_lshl_add_u64 v[12:13], s[14:15], 0, v[198:199]
	global_load_lds_dwordx4 v[12:13], off
	v_lshl_add_u64 v[12:13], s[14:15], 0, v[202:203]
	s_add_i32 m0, s58, 0x1a000
	s_add_i32 s72, s58, 0x8000
	s_add_i32 s84, s58, 0xa000
	global_load_lds_dwordx4 v[12:13], off
	v_lshl_add_u64 v[2:3], v[2:3], 0, s[60:61]
	s_mov_b32 m0, s72
	s_add_u32 s10, s11, 0x840080
	global_load_lds_dwordx4 v[2:3], off
	v_lshl_add_u64 v[2:3], v[4:5], 0, s[60:61]
	s_mov_b32 m0, s84
	s_addc_u32 s11, s12, 0
	global_load_lds_dwordx4 v[2:3], off
	s_add_i32 m0, s58, 0x1c000
	v_lshl_add_u64 v[2:3], s[10:11], 0, v[198:199]
	global_load_lds_dwordx4 v[2:3], off
	v_lshl_add_u64 v[2:3], s[10:11], 0, v[202:203]
	s_add_i32 m0, s58, 0x1e000
	s_cmpk_lt_u32 s8, 0x100
	global_load_lds_dwordx4 v[2:3], off
	s_mov_b64 vcc, s[34:35]
	s_cbranch_vccz .Lpro_skip_2
	s_barrier
.Lpro_skip_2:
	s_waitcnt vmcnt(8)
	s_barrier
	v_lshlrev_b32_e32 v2, 14, v6
	v_and_b32_e32 v2, 0xffff8000, v2
	v_lshl_add_u32 v2, v7, 11, v2
	v_and_b32_e32 v3, 1, v6
	v_lshl_or_b32 v2, v3, 6, v2
	v_lshl_add_u32 v208, v8, 1, v2
	v_lshlrev_b32_e32 v2, 14, v9
	v_and_b32_e32 v2, 0xffff8000, v2
	s_waitcnt vmcnt(6)
	v_lshl_add_u32 v2, v10, 11, v2
	v_and_b32_e32 v3, 1, v9
	v_lshl_or_b32 v2, v3, 6, v2
	s_cselect_b64 s[38:39], -1, 0
	v_lshl_or_b32 v225, s26, 5, v15
	v_mov_b32_e32 v209, v67
	v_lshl_add_u32 v210, v11, 1, v2
	v_mov_b32_e32 v211, v67
	s_mov_b64 s[50:51], 0
	v_add_u32_e32 v226, 0, v14
	s_mov_b64 s[42:43], s[36:37]
	s_mov_b64 s[40:41], s[46:47]
	s_barrier
	s_branch .LBB0_504

.LBB0_672:
	v_bfe_u32 v13, v12, 4, 2
	v_and_b32_e32 v14, 15, v12
	v_lshlrev_b32_e32 v15, 3, v13
	v_lshlrev_b32_e32 v13, 4, v13
	v_lshlrev_b32_e32 v12, 2, v12
	s_and_b32 s26, s10, 3
	v_lshl_or_b32 v205, s9, 6, v14
	v_lshl_or_b32 v13, v14, 6, v13
	s_lshl_b32 s9, s9, 13
	v_and_b32_e32 v12, 32, v12
	v_bitop3_b32 v14, v13, s9, v12 bitop3:0xde
	s_lshl_b32 s9, s26, 12
	s_lshl_b32 s87, s13, 8
	s_lshl_b32 s88, s14, 8
	s_add_u32 s14, s11, 0x800080
	v_mov_b32_e32 v197, v67
	s_addc_u32 s15, s12, 0
	v_mov_b32_e32 v201, v67
	v_bitop3_b32 v222, v13, s9, v12 bitop3:0xde
	s_add_i32 m0, s58, 0x18000
	v_lshl_add_u64 v[12:13], s[14:15], 0, v[196:197]
	global_load_lds_dwordx4 v[12:13], off
	v_lshl_add_u64 v[12:13], s[14:15], 0, v[200:201]
	s_add_i32 m0, s58, 0x1a000
	s_add_i32 s72, s58, 0x8000
	s_add_i32 s84, s58, 0xa000
	global_load_lds_dwordx4 v[12:13], off
	v_lshl_add_u64 v[2:3], v[2:3], 0, s[60:61]
	s_mov_b32 m0, s72
	s_add_u32 s10, s11, 0x840080
	global_load_lds_dwordx4 v[2:3], off
	v_lshl_add_u64 v[2:3], v[4:5], 0, s[60:61]
	s_mov_b32 m0, s84
	s_addc_u32 s11, s12, 0
	global_load_lds_dwordx4 v[2:3], off
	s_add_i32 m0, s58, 0x1c000
	v_lshl_add_u64 v[2:3], s[10:11], 0, v[196:197]
	global_load_lds_dwordx4 v[2:3], off
	v_lshl_add_u64 v[2:3], s[10:11], 0, v[200:201]
	s_add_i32 m0, s58, 0x1e000
	s_cmpk_lt_u32 s8, 0x100
	global_load_lds_dwordx4 v[2:3], off
	s_mov_b64 vcc, s[34:35]
	s_cbranch_vccz .Lpro_skip_3
	s_barrier
.Lpro_skip_3:
	s_waitcnt vmcnt(8)
	s_barrier
	v_lshlrev_b32_e32 v2, 14, v6
	v_and_b32_e32 v2, 0xffff8000, v2
	v_lshl_add_u32 v2, v7, 11, v2
	v_and_b32_e32 v3, 1, v6
	v_lshl_or_b32 v2, v3, 6, v2
	v_lshl_add_u32 v202, v8, 1, v2
	v_lshlrev_b32_e32 v2, 14, v9
	v_and_b32_e32 v2, 0xffff8000, v2
	s_waitcnt vmcnt(6)
	v_lshl_add_u32 v2, v10, 11, v2
	v_and_b32_e32 v3, 1, v9
	v_lshl_or_b32 v2, v3, 6, v2
	s_cselect_b64 s[38:39], -1, 0
	v_lshl_or_b32 v223, s26, 5, v15
	v_mov_b32_e32 v203, v67
	v_lshl_add_u32 v208, v11, 1, v2
	v_mov_b32_e32 v209, v67
	s_mov_b64 s[50:51], 0
	v_add_u32_e32 v224, 0, v14
	s_mov_b64 s[42:43], s[36:37]
	s_mov_b64 s[40:41], s[46:47]
	s_barrier
	s_branch .LBB0_675

.LBB0_785:
	s_or_b64 exec, exec, s[36:37]
	s_mov_b64 s[26:27], exec
	v_mbcnt_lo_u32_b32 v2, s26, 0
	v_mbcnt_hi_u32_b32 v2, s27, v2
	v_cmp_eq_u32_e32 vcc, 0, v2
	s_waitcnt vmcnt(0)
	s_and_saveexec_b64 s[36:37], vcc
	s_cbranch_execz .LBB0_787
	s_bcnt1_i32_b64 s2, s[26:27]
	v_mov_b32_e32 v2, s2
	v_readlane_b32 s2, v254, 7
	v_readlane_b32 s3, v254, 8
	s_nop 4
	global_atomic_add v67, v2, s[2:3]
	buffer_inv sc1

.LBB0_793:
	v_bfe_u32 v17, v16, 4, 2
	v_and_b32_e32 v205, 15, v16
	v_lshlrev_b32_e32 v224, 4, v17
	v_lshlrev_b32_e32 v16, 2, v16
	s_and_b32 s14, s10, 3
	v_lshl_or_b32 v18, v205, 6, v224
	s_lshl_b32 s10, s9, 13
	v_and_b32_e32 v16, 32, v16
	v_bitop3_b32 v19, v18, s10, v16 bitop3:0xde
	s_lshl_b32 s10, s42, 8
	s_lshl_b32 s13, s13, 9
	s_lshl_b32 s12, s12, 1
	s_add_i32 m0, s74, 0x18000
	v_lshl_add_u64 v[8:9], v[8:9], 0, s[60:61]
	s_lshl_b32 s90, s9, 6
	s_lshl_b32 s15, s14, 12
	s_or_b32 s34, s10, s13
	s_or_b32 s43, s12, s11
	global_load_lds_dwordx4 v[8:9], off
	v_lshl_add_u64 v[6:7], v[6:7], 0, s[60:61]
	s_add_i32 m0, s74, 0x1a000
	s_add_i32 s91, s74, 0x8000
	s_add_i32 s92, s74, 0xa000
	global_load_lds_dwordx4 v[6:7], off
	v_lshl_add_u64 v[2:3], v[2:3], 0, s[60:61]
	s_mov_b32 m0, s91
	s_add_u32 s10, s36, 0x40080
	global_load_lds_dwordx4 v[2:3], off
	v_lshl_add_u64 v[2:3], v[4:5], 0, s[60:61]
	s_mov_b32 m0, s92
	s_addc_u32 s11, s37, 0
	global_load_lds_dwordx4 v[2:3], off
	s_add_i32 m0, s74, 0x1c000
	v_lshl_add_u64 v[2:3], s[10:11], 0, v[198:199]
	global_load_lds_dwordx4 v[2:3], off
	v_lshl_add_u64 v[2:3], s[10:11], 0, v[202:203]
	s_add_i32 m0, s74, 0x1e000
	v_and_b32_e32 v4, 1, v10
	global_load_lds_dwordx4 v[2:3], off
	s_mov_b64 vcc, s[46:47]
	s_cbranch_vccz .Lpro_skip_4
	s_barrier
.Lpro_skip_4:
	s_waitcnt vmcnt(8)
	s_barrier
	v_lshlrev_b32_e32 v3, 16, v10
	v_and_b32_e32 v3, 0xfffe0000, v3
	v_lshl_add_u32 v3, v11, 13, v3
	s_cmpk_lt_u32 s8, 0x100
	v_lshl_or_b32 v3, v4, 6, v3
	s_cselect_b64 s[48:49], -1, 0
	s_and_b32 s8, s8, 0xffffff00
	s_lshl_b32 s10, s14, 6
	v_lshl_add_u32 v208, v12, 1, v3
	v_lshlrev_b32_e32 v3, 16, v13
	s_or_b32 s93, s10, s8
	s_lshl_b32 s8, s9, 11
	s_lshl_b32 s9, s14, 3
	v_and_b32_e32 v3, 0xfffe0000, v3
	v_lshlrev_b32_e32 v20, 3, v17
	s_waitcnt vmcnt(6)
	s_add_i32 s9, s9, 0
	v_lshl_add_u32 v3, v14, 13, v3
	v_and_b32_e32 v4, 1, v13
	v_lshl_or_b32 v2, s14, 5, v20
	s_add_i32 s94, s9, s8
	v_lshl_or_b32 v3, v4, 6, v3
	v_bitop3_b32 v225, v18, s15, v16 bitop3:0xde
	v_cmp_eq_u32_e64 s[38:39], 0, v17
	s_add_i32 s94, s94, 0x25000
	s_lshl_b32 s95, s33, 8
	v_mov_b32_e32 v209, v67
	v_lshl_add_u32 v210, v15, 1, v3
	v_mov_b32_e32 v211, v67
	s_mov_b64 s[64:65], 0
	v_lshlrev_b32_e32 v66, 1, v2
	v_add_u32_e32 v226, 0, v19
	s_mov_b64 s[54:55], s[36:37]
	s_mov_b64 s[52:53], s[40:41]
	s_barrier
	s_branch .LBB0_796

.LBB0_905:
	v_lshrrev_b32_e32 v18, 1, v8
	v_and_b32_e32 v18, 24, v18
	s_lshl_b32 s10, s10, 5
	v_and_b32_e32 v9, 15, v8
	v_lshlrev_b32_e32 v19, 1, v18
	v_lshlrev_b32_e32 v8, 2, v8
	s_and_b32 s12, s10, 0x60
	v_lshl_add_u64 v[10:11], s[36:37], 0, v[66:67]
	v_mov_b32_e32 v137, v67
	v_lshl_or_b32 v146, s9, 6, v9
	v_lshl_or_b32 v9, v9, 6, v19
	v_and_b32_e32 v8, 32, v8
	s_lshl_b32 s9, s9, 13
	s_lshl_b32 s10, s12, 7
	v_lshl_add_u64 v[12:13], s[36:37], 0, v[136:137]
	v_mov_b32_e32 v133, v67
	v_bitop3_b32 v147, v9, s10, v8 bitop3:0xde
	v_bitop3_b32 v19, v9, s9, v8 bitop3:0xde
	s_add_i32 m0, s59, 0x18000
	v_lshl_add_u64 v[8:9], v[10:11], 0, s[60:61]
	v_lshl_add_u64 v[14:15], s[52:53], 0, v[132:133]
	v_mov_b32_e32 v135, v67
	global_load_lds_dwordx4 v[8:9], off
	v_lshl_add_u64 v[8:9], v[12:13], 0, s[60:61]
	s_add_i32 m0, s59, 0x1a000
	s_add_i32 s67, s59, 0x8000
	s_add_i32 s68, s59, 0xa000
	v_lshl_add_u64 v[16:17], s[52:53], 0, v[134:135]
	global_load_lds_dwordx4 v[8:9], off
	v_lshl_add_u64 v[8:9], v[14:15], 0, s[60:61]
	s_mov_b32 m0, s67
	s_add_u32 s10, s36, 0x80080
	global_load_lds_dwordx4 v[8:9], off
	v_lshl_add_u64 v[8:9], v[16:17], 0, s[60:61]
	s_mov_b32 m0, s68
	s_addc_u32 s11, s37, 0
	global_load_lds_dwordx4 v[8:9], off
	s_add_i32 m0, s59, 0x1c000
	v_lshl_add_u64 v[8:9], s[10:11], 0, v[66:67]
	global_load_lds_dwordx4 v[8:9], off
	v_lshl_add_u64 v[8:9], s[10:11], 0, v[136:137]
	s_add_i32 m0, s59, 0x1e000
	s_cmpk_lt_u32 s8, 0x100
	global_load_lds_dwordx4 v[8:9], off
	s_mov_b64 vcc, s[42:43]
	s_cbranch_vccz .Lpro_skip_5
	s_barrier
.Lpro_skip_5:
	s_waitcnt vmcnt(8)
	s_barrier
	v_lshlrev_b32_e32 v8, 15, v2
	v_and_b32_e32 v8, 0xffff0000, v8
	v_lshl_add_u32 v3, v3, 12, v8
	v_and_b32_e32 v2, 1, v2
	v_lshl_or_b32 v2, v2, 6, v3
	v_lshl_add_u32 v138, v4, 1, v2
	v_lshlrev_b32_e32 v2, 15, v5
	v_and_b32_e32 v2, 0xffff0000, v2
	s_waitcnt vmcnt(6)
	v_lshl_add_u32 v2, v6, 12, v2
	v_and_b32_e32 v3, 1, v5
	v_lshl_or_b32 v2, v3, 6, v2
	s_cselect_b64 s[44:45], -1, 0
	v_or_b32_e32 v148, s12, v18
	v_mov_b32_e32 v139, v67
	v_lshl_add_u32 v140, v7, 1, v2
	v_mov_b32_e32 v141, v67
	v_add_u32_e32 v149, 0, v19
	s_mov_b64 s[48:49], s[36:37]
	s_mov_b64 s[46:47], s[52:53]
	s_barrier
	s_branch .LBB0_908

.LBB0_921:
	v_lshrrev_b32_e32 v18, 1, v8
	v_and_b32_e32 v18, 24, v18
	s_lshl_b32 s10, s10, 5
	v_and_b32_e32 v9, 15, v8
	v_lshlrev_b32_e32 v19, 1, v18
	v_lshlrev_b32_e32 v8, 2, v8
	s_and_b32 s12, s10, 0x60
	v_lshl_add_u64 v[10:11], s[36:37], 0, v[66:67]
	v_mov_b32_e32 v157, v67
	v_lshl_or_b32 v170, s9, 6, v9
	v_lshl_or_b32 v9, v9, 6, v19
	v_and_b32_e32 v8, 32, v8
	s_lshl_b32 s9, s9, 13
	s_lshl_b32 s10, s12, 7
	v_lshl_add_u64 v[12:13], s[36:37], 0, v[156:157]
	v_mov_b32_e32 v153, v67
	v_bitop3_b32 v171, v9, s10, v8 bitop3:0xde
	v_bitop3_b32 v19, v9, s9, v8 bitop3:0xde
	s_add_i32 m0, s55, 0x18000
	v_lshl_add_u64 v[8:9], v[10:11], 0, s[60:61]
	v_lshl_add_u64 v[14:15], s[50:51], 0, v[152:153]
	v_mov_b32_e32 v155, v67
	global_load_lds_dwordx4 v[8:9], off
	v_lshl_add_u64 v[8:9], v[12:13], 0, s[60:61]
	s_add_i32 m0, s55, 0x1a000
	s_add_i32 s59, s55, 0x8000
	s_add_i32 s64, s55, 0xa000
	v_lshl_add_u64 v[16:17], s[50:51], 0, v[154:155]
	global_load_lds_dwordx4 v[8:9], off
	v_lshl_add_u64 v[8:9], v[14:15], 0, s[60:61]
	s_mov_b32 m0, s59
	s_add_u32 s10, s36, 0x40080
	global_load_lds_dwordx4 v[8:9], off
	v_lshl_add_u64 v[8:9], v[16:17], 0, s[60:61]
	s_mov_b32 m0, s64
	s_addc_u32 s11, s37, 0
	global_load_lds_dwordx4 v[8:9], off
	s_add_i32 m0, s55, 0x1c000
	v_lshl_add_u64 v[8:9], s[10:11], 0, v[66:67]
	global_load_lds_dwordx4 v[8:9], off
	v_lshl_add_u64 v[8:9], s[10:11], 0, v[156:157]
	s_add_i32 m0, s55, 0x1e000
	s_cmpk_lt_u32 s8, 0x100
	global_load_lds_dwordx4 v[8:9], off
	s_mov_b64 vcc, s[34:35]
	s_cbranch_vccz .Lpro_skip_6
	s_barrier
.Lpro_skip_6:
	s_waitcnt vmcnt(8)
	s_barrier
	v_lshlrev_b32_e32 v8, 14, v2
	v_and_b32_e32 v8, 0xffff8000, v8
	v_lshl_add_u32 v3, v3, 11, v8
	v_and_b32_e32 v2, 1, v2
	v_lshl_or_b32 v2, v2, 6, v3
	v_lshl_add_u32 v158, v4, 1, v2
	v_lshlrev_b32_e32 v2, 14, v5
	v_and_b32_e32 v2, 0xffff8000, v2
	s_waitcnt vmcnt(6)
	v_lshl_add_u32 v2, v6, 11, v2
	v_and_b32_e32 v3, 1, v5
	v_lshl_or_b32 v2, v3, 6, v2
	s_cselect_b64 s[42:43], -1, 0
	v_or_b32_e32 v172, s12, v18
	v_mov_b32_e32 v159, v67
	v_lshl_add_u32 v160, v7, 1, v2
	v_mov_b32_e32 v161, v67
	v_add_u32_e32 v173, 0, v19
	s_mov_b64 s[46:47], s[36:37]
	s_mov_b64 s[44:45], s[50:51]
	s_barrier
	s_branch .LBB0_924

.LBB0_992:
	v_bfe_u32 v17, v16, 4, 2
	s_and_b32 s54, s10, 3
	v_and_b32_e32 v216, 15, v16
	v_lshlrev_b32_e32 v217, 4, v17
	v_lshlrev_b32_e32 v16, 2, v16
	v_lshl_or_b32 v18, v216, 6, v217
	v_and_b32_e32 v16, 32, v16
	s_lshl_b32 s10, s54, 12
	s_lshl_b32 s89, s9, 6
	s_lshl_b32 s55, s9, 13
	v_bitop3_b32 v218, v18, s10, v16 bitop3:0xde
	s_lshl_b32 s10, s33, 17
	s_add_u32 s10, s44, s10
	s_addc_u32 s11, s45, 0
	s_lshl_b32 s72, s33, 10
	s_lshl_b64 s[12:13], s[72:73], 2
	s_waitcnt lgkmcnt(0)
	s_add_u32 s14, s40, s12
	s_addc_u32 s15, s41, s13
	s_add_u32 s12, s42, s12
	s_addc_u32 s13, s43, s13
	s_add_i32 m0, s85, 0x18000
	v_lshl_add_u64 v[8:9], v[8:9], 0, s[60:61]
	global_load_lds_dwordx4 v[8:9], off
	v_lshl_add_u64 v[6:7], v[6:7], 0, s[60:61]
	s_add_i32 m0, s85, 0x1a000
	s_add_i32 s72, s85, 0x8000
	s_add_i32 s90, s85, 0xa000
	global_load_lds_dwordx4 v[6:7], off
	v_lshl_add_u64 v[2:3], v[2:3], 0, s[60:61]
	s_mov_b32 m0, s72
	s_add_u32 s26, s36, 0x40080
	global_load_lds_dwordx4 v[2:3], off
	v_lshl_add_u64 v[2:3], v[4:5], 0, s[60:61]
	s_mov_b32 m0, s90
	s_addc_u32 s27, s37, 0
	global_load_lds_dwordx4 v[2:3], off
	s_add_i32 m0, s85, 0x1c000
	v_lshl_add_u64 v[2:3], s[26:27], 0, v[174:175]
	global_load_lds_dwordx4 v[2:3], off
	v_lshl_add_u64 v[2:3], s[26:27], 0, v[178:179]
	s_add_i32 m0, s85, 0x1e000
	v_lshlrev_b32_e32 v20, 3, v17
	global_load_lds_dwordx4 v[2:3], off
	s_mov_b64 vcc, s[50:51]
	s_cbranch_vccz .Lpro_skip_7
	s_barrier
.Lpro_skip_7:
	s_waitcnt vmcnt(8)
	s_barrier
	s_cmpk_lt_u32 s8, 0x100
	v_lshl_or_b32 v2, s54, 5, v20
	s_cselect_b64 s[52:53], -1, 0
	s_and_b32 s8, s8, 0xffffff00
	s_lshl_b32 s26, s54, 6
	v_lshlrev_b32_e32 v66, 1, v2
	v_lshlrev_b32_e32 v3, 14, v10
	s_or_b32 s91, s26, s8
	s_lshl_b32 s27, s9, 11
	v_lshl_add_u64 v[4:5], s[10:11], 0, v[66:67]
	s_mov_b64 s[8:9], 0xb00000
	v_and_b32_e32 v3, 0xffff8000, v3
	v_lshl_add_u64 v[180:181], v[4:5], 0, s[8:9]
	v_lshl_add_u32 v3, v11, 11, v3
	v_and_b32_e32 v4, 1, v10
	v_lshl_or_b32 v3, v4, 6, v3
	v_lshl_add_u32 v186, v12, 1, v3
	v_lshlrev_b32_e32 v3, 14, v13
	s_lshl_b32 s8, s54, 3
	v_and_b32_e32 v3, 0xffff8000, v3
	s_waitcnt vmcnt(6)
	s_add_i32 s8, s8, 0
	v_lshl_add_u32 v3, v14, 11, v3
	v_and_b32_e32 v4, 1, v13
	v_bitop3_b32 v19, v18, s55, v16 bitop3:0xde
	s_lshl_b32 s26, s54, 15
	v_lshlrev_b32_e32 v66, 2, v2
	s_add_i32 s93, s8, s27
	s_add_i32 s92, s55, 0
	v_lshl_or_b32 v3, v4, 6, v3
	v_cmp_eq_u32_e64 s[38:39], 0, v17
	v_lshl_add_u64 v[182:183], s[14:15], 0, v[66:67]
	v_lshl_add_u64 v[184:185], s[12:13], 0, v[66:67]
	s_add_i32 s92, s92, s26
	s_add_i32 s93, s93, 0x25000
	v_mov_b32_e32 v187, v67
	v_lshl_add_u32 v188, v15, 1, v3
	v_mov_b32_e32 v189, v67
	v_add_u32_e32 v219, 0, v19
	v_lshlrev_b32_e32 v66, 1, v2
	s_mov_b64 s[56:57], s[36:37]
	s_mov_b64 s[54:55], s[34:35]
	s_barrier
	s_branch .LBB0_995

.LBB0_1228:
	v_lshrrev_b32_e32 v10, 1, v8
	v_ashrrev_i32_e32 v9, 2, v9
	v_and_b32_e32 v10, 24, v10
	v_lshlrev_b32_e32 v242, 8, v9
	v_and_b32_e32 v9, 15, v8
	v_lshlrev_b32_e32 v11, 1, v10
	v_lshlrev_b32_e32 v8, 2, v8
	s_lshl_b32 s9, s9, 5
	v_lshl_or_b32 v235, s10, 6, v9
	v_lshl_or_b32 v9, v9, 6, v11
	s_lshl_b32 s10, s10, 13
	v_and_b32_e32 v8, 32, v8
	s_and_b32 s9, s9, 0x60
	v_bitop3_b32 v11, v9, s10, v8 bitop3:0xde
	s_lshl_b32 s10, s9, 7
	s_add_u32 s74, s58, 0x16a00000
	s_addc_u32 s75, s59, 0
	s_add_u32 s48, s58, 0xca00080
	s_addc_u32 s49, s59, 0
	s_add_i32 m0, s90, 0x18000
	v_lshl_add_u64 v[4:5], v[4:5], 0, s[60:61]
	v_mov_b32_e32 v211, v67
	global_load_lds_dwordx4 v[4:5], off
	v_lshl_add_u64 v[4:5], v[6:7], 0, s[60:61]
	s_add_i32 m0, s90, 0x1a000
	s_add_i32 s56, s90, 0x8000
	v_mov_b32_e32 v215, v67
	global_load_lds_dwordx4 v[4:5], off
	v_lshl_add_u64 v[4:5], s[48:49], 0, v[210:211]
	s_mov_b32 m0, s56
	s_add_i32 s57, s90, 0xa000
	global_load_lds_dwordx4 v[4:5], off
	v_lshl_add_u64 v[4:5], s[48:49], 0, v[214:215]
	s_mov_b32 m0, s57
	v_bitop3_b32 v236, v9, s10, v8 bitop3:0xde
	global_load_lds_dwordx4 v[4:5], off
	v_lshl_add_u64 v[4:5], v[2:3], 0, s[30:31]
	s_add_i32 m0, s90, 0x1c000
	v_lshl_add_u64 v[6:7], v[4:5], 0, v[196:197]
	global_load_lds_dwordx4 v[6:7], off
	v_lshl_add_u64 v[4:5], v[4:5], 0, v[198:199]
	s_add_i32 m0, s90, 0x1e000
	s_cmpk_lt_u32 s8, 0x100
	global_load_lds_dwordx4 v[4:5], off
	s_mov_b64 vcc, s[70:71]
	s_cbranch_vccz .Lpro_skip_8
	s_barrier
.Lpro_skip_8:
	s_waitcnt vmcnt(8)
	s_barrier
	s_waitcnt vmcnt(6)
	v_or_b32_e32 v4, s9, v10
	s_cselect_b64 s[50:51], -1, 0
	s_mov_b32 s44, 0
	s_mov_b64 s[34:35], 0
	v_lshlrev_b32_e32 v200, 1, v4
	v_add_u32_e32 v211, 0, v11
	v_mov_b64_e32 v[202:203], v[2:3]
	s_barrier
	s_branch .LBB0_1231

.LBB0_1471:
	v_lshrrev_b32_e32 v20, 1, v11
	v_and_b32_e32 v20, 24, v20
	v_and_b32_e32 v15, 15, v11
	v_lshlrev_b32_e32 v21, 1, v20
	v_lshlrev_b32_e32 v11, 2, v11
	s_lshl_b32 s9, s9, 5
	v_lshl_or_b32 v230, s10, 6, v15
	v_lshl_or_b32 v15, v15, 6, v21
	s_lshl_b32 s10, s10, 13
	v_and_b32_e32 v11, 32, v11
	s_and_b32 s9, s9, 0x60
	v_mov_b32_e32 v199, v67
	s_lshl_b32 s47, s36, 8
	v_bitop3_b32 v21, v15, s10, v11 bitop3:0xde
	s_lshl_b32 s10, s9, 7
	s_waitcnt vmcnt(0)
	v_lshl_add_u64 v[16:17], v[2:3], 0, v[198:199]
	v_mov_b32_e32 v203, v67
	s_add_u32 s64, s52, 0x19200000
	v_lshl_add_u64 v[18:19], v[2:3], 0, v[202:203]
	s_addc_u32 s65, s53, 0
	s_add_i32 m0, s92, 0x18000
	v_lshl_add_u64 v[16:17], v[16:17], 0, s[60:61]
	global_load_lds_dwordx4 v[16:17], off
	v_lshl_add_u64 v[16:17], v[18:19], 0, s[60:61]
	s_add_i32 m0, s92, 0x1a000
	s_add_i32 s48, s92, 0x8000
	global_load_lds_dwordx4 v[16:17], off
	v_lshl_add_u64 v[4:5], v[4:5], 0, s[60:61]
	s_mov_b32 m0, s48
	s_add_i32 s49, s92, 0xa000
	global_load_lds_dwordx4 v[4:5], off
	v_lshl_add_u64 v[4:5], v[6:7], 0, s[60:61]
	s_mov_b32 m0, s49
	v_bitop3_b32 v231, v15, s10, v11 bitop3:0xde
	global_load_lds_dwordx4 v[4:5], off
	v_lshl_add_u64 v[4:5], v[2:3], 0, s[62:63]
	s_add_i32 m0, s92, 0x1c000
	v_lshl_add_u64 v[6:7], v[4:5], 0, v[198:199]
	global_load_lds_dwordx4 v[6:7], off
	v_lshl_add_u64 v[4:5], v[4:5], 0, v[202:203]
	s_add_i32 m0, s92, 0x1e000
	v_and_b32_e32 v6, 1, v8
	global_load_lds_dwordx4 v[4:5], off
	s_mov_b64 vcc, s[58:59]
	s_cbranch_vccz .Lpro_skip_9
	s_barrier
.Lpro_skip_9:
	s_waitcnt vmcnt(8)
	s_barrier
	v_lshlrev_b32_e32 v5, 13, v8
	v_and_b32_e32 v5, 0xffffc000, v5
	v_lshl_add_u32 v5, v9, 10, v5
	v_lshl_or_b32 v5, v6, 6, v5
	v_lshl_add_u32 v208, v10, 1, v5
	v_lshlrev_b32_e32 v5, 13, v12
	v_and_b32_e32 v5, 0xffffc000, v5
	s_waitcnt vmcnt(6)
	v_lshl_add_u32 v5, v13, 10, v5
	v_and_b32_e32 v6, 1, v12
	s_cmpk_lt_u32 s8, 0x100
	v_or_b32_e32 v4, s9, v20
	v_lshl_or_b32 v5, v6, 6, v5
	s_cselect_b64 s[66:67], -1, 0
	v_mov_b32_e32 v209, v67
	v_lshl_add_u32 v210, v14, 1, v5
	v_mov_b32_e32 v211, v67
	s_mov_b64 s[36:37], 0
	v_lshlrev_b32_e32 v66, 1, v4
	v_add_u32_e32 v232, 0, v21
	v_mov_b64_e32 v[212:213], v[2:3]
	s_mov_b64 s[70:71], s[74:75]
	s_barrier
	s_branch .LBB0_1474

.LBB0_1796:
	s_or_b64 exec, exec, s[36:37]
	s_mov_b64 s[26:27], exec
	v_mbcnt_lo_u32_b32 v2, s26, 0
	v_mbcnt_hi_u32_b32 v2, s27, v2
	v_cmp_eq_u32_e32 vcc, 0, v2
	s_waitcnt vmcnt(0)
	s_and_saveexec_b64 s[36:37], vcc
	s_cbranch_execnz .LBB0_1797
	s_getpc_b64 s[98:99]

.LBB0_1797:
	s_bcnt1_i32_b64 s2, s[26:27]
	v_mov_b32_e32 v2, s2
	v_readlane_b32 s2, v254, 7
	v_readlane_b32 s3, v254, 8
	s_nop 4
	global_atomic_add v67, v2, s[2:3]
	buffer_inv sc1
	s_getpc_b64 s[98:99]
